# attention epilogue: in-quad 4x4 transpose (cndmask+DPP) and 16 dwordx2 stores per lane instead of 64 short stores (1)
# speedup vs baseline: 1.0041x; 1.0041x over previous
; __device__ __forceinline__ bf16_t f2bf(float f) { return (bf16_t)(cvt_pk_bf16(f, 0.f) & 0xffffu); }
; __device__ __forceinline__ int crow(int r, int hi) { return (r & 3) + 8 * (r >> 2) + 4 * hi; }
; __device__ __forceinline__ void attn_dense_body(const bf16_t* __restrict__ Qb, const bf16_t* __restrict__ Kh, const bf16_t* __restrict__ Vh, bf16_t* __restrict__ Ob, int seq, char* lds) {
;     ...
;   if (hi == 0) li_l[r32] = l_reg; asm volatile("s_waitcnt lgkmcnt(0)" ::: "memory");
;   float rli[16];
; #pragma unroll
;   for (int r = 0; r < 16; ++r) rli[r] = __builtin_amdgcn_rcpf(li_l[crow(r, hi)]);
;   bf16_t* Ow = Ob + (long)(wid * QBLK) * LDO;
; #pragma unroll
;   for (int r = 0; r < 16; ++r) { int orow = crow(r, hi);
;     for (int d0 = 0; d0 < 4; ++d0) Ow[(long)orow * LDO + d0 * 32 + r32] = f2bf(o[d0][r] * rli[r]); }
.LBB0_705:
	s_or_b64 exec, exec, s[4:5]
	s_waitcnt lgkmcnt(0)
	v_add_u32_e32 v82, v192, v180
	ds_read_b128 v[66:69], v82
	ds_read_b128 v[70:73], v82 offset:32
	ds_read_b128 v[74:77], v82 offset:64
	ds_read_b128 v[78:81], v82 offset:96
	s_mov_b32 s101, 0
	v_lshl_add_u64 v[250:251], s[12:13], 1, v[184:185]
	v_and_b32_e32 v248, 3, v0
	v_mul_u32_u24_e32 v248, 0x7fe, v248
	v_mov_b32_e32 v249, 0
	s_nop 0
	v_lshl_add_u64 v[250:251], v[248:249], 0, v[250:251]
	s_waitcnt lgkmcnt(0)
	v_rcp_f32_e32 v66, v66
	v_rcp_f32_e32 v67, v67
	v_rcp_f32_e32 v68, v68
	v_rcp_f32_e32 v69, v69
	v_rcp_f32_e32 v70, v70
	v_rcp_f32_e32 v71, v71
	v_rcp_f32_e32 v72, v72
	v_rcp_f32_e32 v73, v73
	v_rcp_f32_e32 v74, v74
	v_rcp_f32_e32 v75, v75
	v_rcp_f32_e32 v76, v76
	v_rcp_f32_e32 v77, v77
	v_rcp_f32_e32 v78, v78
	v_rcp_f32_e32 v79, v79
	v_rcp_f32_e32 v80, v80
	v_rcp_f32_e32 v81, v81
	v_mul_f32_e32 v2, v2, v66
	v_mul_f32_e32 v3, v3, v67
	v_mul_f32_e32 v4, v4, v68
	v_mul_f32_e32 v5, v5, v69
	v_mul_f32_e32 v50, v50, v66
	v_mul_f32_e32 v51, v51, v67
	v_mul_f32_e32 v52, v52, v68
	v_mul_f32_e32 v53, v53, v69
	s_mov_b32 vcc_lo, 0xaaaaaaaa
	s_mov_b32 vcc_hi, 0xaaaaaaaa
	s_nop 1
	v_mov_b32_e32 v82, v3
	v_mov_b32_e32 v83, v5
	v_mov_b32_e32 v254, v51
	v_mov_b32_e32 v255, v53
	v_cndmask_b32_dpp v3, v2, v3, vcc quad_perm:[1,0,3,2] row_mask:0xf bank_mask:0xf
	v_cndmask_b32_dpp v5, v4, v5, vcc quad_perm:[1,0,3,2] row_mask:0xf bank_mask:0xf
	v_cndmask_b32_dpp v51, v50, v51, vcc quad_perm:[1,0,3,2] row_mask:0xf bank_mask:0xf
	v_cndmask_b32_dpp v53, v52, v53, vcc quad_perm:[1,0,3,2] row_mask:0xf bank_mask:0xf
	s_mov_b32 vcc_lo, 0x55555555
	s_mov_b32 vcc_hi, 0x55555555
	s_nop 1
	v_cndmask_b32_dpp v2, v82, v2, vcc quad_perm:[1,0,3,2] row_mask:0xf bank_mask:0xf
	v_cndmask_b32_dpp v4, v83, v4, vcc quad_perm:[1,0,3,2] row_mask:0xf bank_mask:0xf
	v_cndmask_b32_dpp v50, v254, v50, vcc quad_perm:[1,0,3,2] row_mask:0xf bank_mask:0xf
	v_cndmask_b32_dpp v52, v255, v52, vcc quad_perm:[1,0,3,2] row_mask:0xf bank_mask:0xf
	s_mov_b32 vcc_lo, 0xcccccccc
	s_mov_b32 vcc_hi, 0xcccccccc
	s_nop 1
	v_mov_b32_e32 v82, v4
	v_mov_b32_e32 v83, v5
	v_mov_b32_e32 v254, v52
	v_mov_b32_e32 v255, v53
	v_cndmask_b32_dpp v4, v2, v4, vcc quad_perm:[2,3,0,1] row_mask:0xf bank_mask:0xf
	v_cndmask_b32_dpp v5, v3, v5, vcc quad_perm:[2,3,0,1] row_mask:0xf bank_mask:0xf
	v_cndmask_b32_dpp v52, v50, v52, vcc quad_perm:[2,3,0,1] row_mask:0xf bank_mask:0xf
	v_cndmask_b32_dpp v53, v51, v53, vcc quad_perm:[2,3,0,1] row_mask:0xf bank_mask:0xf
	s_mov_b32 vcc_lo, 0x33333333
	s_mov_b32 vcc_hi, 0x33333333
	s_nop 1
	v_cndmask_b32_dpp v2, v82, v2, vcc quad_perm:[2,3,0,1] row_mask:0xf bank_mask:0xf
	v_cndmask_b32_dpp v3, v83, v3, vcc quad_perm:[2,3,0,1] row_mask:0xf bank_mask:0xf
	v_cndmask_b32_dpp v50, v254, v50, vcc quad_perm:[2,3,0,1] row_mask:0xf bank_mask:0xf
	v_cndmask_b32_dpp v51, v255, v51, vcc quad_perm:[2,3,0,1] row_mask:0xf bank_mask:0xf
	v_cvt_pk_bf16_f32 v2, v2, v3
	v_cvt_pk_bf16_f32 v3, v4, v5
	v_cvt_pk_bf16_f32 v50, v50, v51
	v_cvt_pk_bf16_f32 v51, v52, v53
	global_store_dwordx2 v[250:251], v[2:3], off
	global_store_dwordx2 v[250:251], v[50:51], off offset:64
	v_mul_f32_e32 v34, v34, v66
	v_mul_f32_e32 v35, v35, v67
	v_mul_f32_e32 v36, v36, v68
	v_mul_f32_e32 v37, v37, v69
	v_mul_f32_e32 v18, v18, v66
	v_mul_f32_e32 v19, v19, v67
	v_mul_f32_e32 v20, v20, v68
	v_mul_f32_e32 v21, v21, v69
	s_mov_b32 vcc_lo, 0xaaaaaaaa
	s_mov_b32 vcc_hi, 0xaaaaaaaa
	s_nop 1
	v_mov_b32_e32 v82, v35
	v_mov_b32_e32 v83, v37
	v_mov_b32_e32 v254, v19
	v_mov_b32_e32 v255, v21
	v_cndmask_b32_dpp v35, v34, v35, vcc quad_perm:[1,0,3,2] row_mask:0xf bank_mask:0xf
	v_cndmask_b32_dpp v37, v36, v37, vcc quad_perm:[1,0,3,2] row_mask:0xf bank_mask:0xf
	v_cndmask_b32_dpp v19, v18, v19, vcc quad_perm:[1,0,3,2] row_mask:0xf bank_mask:0xf
	v_cndmask_b32_dpp v21, v20, v21, vcc quad_perm:[1,0,3,2] row_mask:0xf bank_mask:0xf
	s_mov_b32 vcc_lo, 0x55555555
	s_mov_b32 vcc_hi, 0x55555555
	s_nop 1
	v_cndmask_b32_dpp v34, v82, v34, vcc quad_perm:[1,0,3,2] row_mask:0xf bank_mask:0xf
	v_cndmask_b32_dpp v36, v83, v36, vcc quad_perm:[1,0,3,2] row_mask:0xf bank_mask:0xf
	v_cndmask_b32_dpp v18, v254, v18, vcc quad_perm:[1,0,3,2] row_mask:0xf bank_mask:0xf
	v_cndmask_b32_dpp v20, v255, v20, vcc quad_perm:[1,0,3,2] row_mask:0xf bank_mask:0xf
	s_mov_b32 vcc_lo, 0xcccccccc
	s_mov_b32 vcc_hi, 0xcccccccc
	s_nop 1
	v_mov_b32_e32 v82, v36
	v_mov_b32_e32 v83, v37
	v_mov_b32_e32 v254, v20
	v_mov_b32_e32 v255, v21
	v_cndmask_b32_dpp v36, v34, v36, vcc quad_perm:[2,3,0,1] row_mask:0xf bank_mask:0xf
	v_cndmask_b32_dpp v37, v35, v37, vcc quad_perm:[2,3,0,1] row_mask:0xf bank_mask:0xf
	v_cndmask_b32_dpp v20, v18, v20, vcc quad_perm:[2,3,0,1] row_mask:0xf bank_mask:0xf
	v_cndmask_b32_dpp v21, v19, v21, vcc quad_perm:[2,3,0,1] row_mask:0xf bank_mask:0xf
	s_mov_b32 vcc_lo, 0x33333333
	s_mov_b32 vcc_hi, 0x33333333
	s_nop 1
	v_cndmask_b32_dpp v34, v82, v34, vcc quad_perm:[2,3,0,1] row_mask:0xf bank_mask:0xf
	v_cndmask_b32_dpp v35, v83, v35, vcc quad_perm:[2,3,0,1] row_mask:0xf bank_mask:0xf
	v_cndmask_b32_dpp v18, v254, v18, vcc quad_perm:[2,3,0,1] row_mask:0xf bank_mask:0xf
	v_cndmask_b32_dpp v19, v255, v19, vcc quad_perm:[2,3,0,1] row_mask:0xf bank_mask:0xf
	v_cvt_pk_bf16_f32 v34, v34, v35
	v_cvt_pk_bf16_f32 v35, v36, v37
	v_cvt_pk_bf16_f32 v18, v18, v19
	v_cvt_pk_bf16_f32 v19, v20, v21
	global_store_dwordx2 v[250:251], v[34:35], off offset:128
	global_store_dwordx2 v[250:251], v[18:19], off offset:192
	s_mov_b32 s100, 0x4000
	v_lshl_add_u64 v[252:253], v[250:251], 0, s[100:101]
	v_mul_f32_e32 v6, v6, v70
	v_mul_f32_e32 v7, v7, v71
	v_mul_f32_e32 v8, v8, v72
	v_mul_f32_e32 v9, v9, v73
; __device__ __forceinline__ bf16_t f2bf(float f) { return (bf16_t)(cvt_pk_bf16(f, 0.f) & 0xffffu); }
; __device__ __forceinline__ int crow(int r, int hi) { return (r & 3) + 8 * (r >> 2) + 4 * hi; }
; __device__ __forceinline__ void attn_dense_body(const bf16_t* __restrict__ Qb, const bf16_t* __restrict__ Kh, const bf16_t* __restrict__ Vh, bf16_t* __restrict__ Ob, int seq, char* lds) {
;     ...
;   bf16_t* Ow = Ob + (long)(wid * QBLK) * LDO;
; #pragma unroll
;   for (int r = 0; r < 16; ++r) { int orow = crow(r, hi);
;     for (int d0 = 0; d0 < 4; ++d0) Ow[(long)orow * LDO + d0 * 32 + r32] = f2bf(o[d0][r] * rli[r]); }
	v_mul_f32_e32 v54, v54, v70
	v_mul_f32_e32 v55, v55, v71
	v_mul_f32_e32 v56, v56, v72
	v_mul_f32_e32 v57, v57, v73
	s_mov_b32 vcc_lo, 0xaaaaaaaa
	s_mov_b32 vcc_hi, 0xaaaaaaaa
	s_nop 1
	v_mov_b32_e32 v82, v7
	v_mov_b32_e32 v83, v9
	v_mov_b32_e32 v254, v55
	v_mov_b32_e32 v255, v57
	v_cndmask_b32_dpp v7, v6, v7, vcc quad_perm:[1,0,3,2] row_mask:0xf bank_mask:0xf
	v_cndmask_b32_dpp v9, v8, v9, vcc quad_perm:[1,0,3,2] row_mask:0xf bank_mask:0xf
	v_cndmask_b32_dpp v55, v54, v55, vcc quad_perm:[1,0,3,2] row_mask:0xf bank_mask:0xf
	v_cndmask_b32_dpp v57, v56, v57, vcc quad_perm:[1,0,3,2] row_mask:0xf bank_mask:0xf
	s_mov_b32 vcc_lo, 0x55555555
	s_mov_b32 vcc_hi, 0x55555555
	s_nop 1
	v_cndmask_b32_dpp v6, v82, v6, vcc quad_perm:[1,0,3,2] row_mask:0xf bank_mask:0xf
	v_cndmask_b32_dpp v8, v83, v8, vcc quad_perm:[1,0,3,2] row_mask:0xf bank_mask:0xf
	v_cndmask_b32_dpp v54, v254, v54, vcc quad_perm:[1,0,3,2] row_mask:0xf bank_mask:0xf
	v_cndmask_b32_dpp v56, v255, v56, vcc quad_perm:[1,0,3,2] row_mask:0xf bank_mask:0xf
	s_mov_b32 vcc_lo, 0xcccccccc
	s_mov_b32 vcc_hi, 0xcccccccc
	s_nop 1
	v_mov_b32_e32 v82, v8
	v_mov_b32_e32 v83, v9
	v_mov_b32_e32 v254, v56
	v_mov_b32_e32 v255, v57
	v_cndmask_b32_dpp v8, v6, v8, vcc quad_perm:[2,3,0,1] row_mask:0xf bank_mask:0xf
	v_cndmask_b32_dpp v9, v7, v9, vcc quad_perm:[2,3,0,1] row_mask:0xf bank_mask:0xf
	v_cndmask_b32_dpp v56, v54, v56, vcc quad_perm:[2,3,0,1] row_mask:0xf bank_mask:0xf
	v_cndmask_b32_dpp v57, v55, v57, vcc quad_perm:[2,3,0,1] row_mask:0xf bank_mask:0xf
	s_mov_b32 vcc_lo, 0x33333333
	s_mov_b32 vcc_hi, 0x33333333
	s_nop 1
	v_cndmask_b32_dpp v6, v82, v6, vcc quad_perm:[2,3,0,1] row_mask:0xf bank_mask:0xf
	v_cndmask_b32_dpp v7, v83, v7, vcc quad_perm:[2,3,0,1] row_mask:0xf bank_mask:0xf
	v_cndmask_b32_dpp v54, v254, v54, vcc quad_perm:[2,3,0,1] row_mask:0xf bank_mask:0xf
	v_cndmask_b32_dpp v55, v255, v55, vcc quad_perm:[2,3,0,1] row_mask:0xf bank_mask:0xf
	v_cvt_pk_bf16_f32 v6, v6, v7
	v_cvt_pk_bf16_f32 v7, v8, v9
	v_cvt_pk_bf16_f32 v54, v54, v55
	v_cvt_pk_bf16_f32 v55, v56, v57
	global_store_dwordx2 v[252:253], v[6:7], off
	global_store_dwordx2 v[252:253], v[54:55], off offset:64
	v_mul_f32_e32 v38, v38, v70
	v_mul_f32_e32 v39, v39, v71
	v_mul_f32_e32 v40, v40, v72
	v_mul_f32_e32 v41, v41, v73
	v_mul_f32_e32 v22, v22, v70
	v_mul_f32_e32 v23, v23, v71
	v_mul_f32_e32 v24, v24, v72
	v_mul_f32_e32 v25, v25, v73
	s_mov_b32 vcc_lo, 0xaaaaaaaa
	s_mov_b32 vcc_hi, 0xaaaaaaaa
	s_nop 1
	v_mov_b32_e32 v82, v39
	v_mov_b32_e32 v83, v41
	v_mov_b32_e32 v254, v23
	v_mov_b32_e32 v255, v25
	v_cndmask_b32_dpp v39, v38, v39, vcc quad_perm:[1,0,3,2] row_mask:0xf bank_mask:0xf
	v_cndmask_b32_dpp v41, v40, v41, vcc quad_perm:[1,0,3,2] row_mask:0xf bank_mask:0xf
	v_cndmask_b32_dpp v23, v22, v23, vcc quad_perm:[1,0,3,2] row_mask:0xf bank_mask:0xf
	v_cndmask_b32_dpp v25, v24, v25, vcc quad_perm:[1,0,3,2] row_mask:0xf bank_mask:0xf
	s_mov_b32 vcc_lo, 0x55555555
	s_mov_b32 vcc_hi, 0x55555555
	s_nop 1
	v_cndmask_b32_dpp v38, v82, v38, vcc quad_perm:[1,0,3,2] row_mask:0xf bank_mask:0xf
	v_cndmask_b32_dpp v40, v83, v40, vcc quad_perm:[1,0,3,2] row_mask:0xf bank_mask:0xf
	v_cndmask_b32_dpp v22, v254, v22, vcc quad_perm:[1,0,3,2] row_mask:0xf bank_mask:0xf
	v_cndmask_b32_dpp v24, v255, v24, vcc quad_perm:[1,0,3,2] row_mask:0xf bank_mask:0xf
	s_mov_b32 vcc_lo, 0xcccccccc
	s_mov_b32 vcc_hi, 0xcccccccc
	s_nop 1
	v_mov_b32_e32 v82, v40
	v_mov_b32_e32 v83, v41
	v_mov_b32_e32 v254, v24
	v_mov_b32_e32 v255, v25
	v_cndmask_b32_dpp v40, v38, v40, vcc quad_perm:[2,3,0,1] row_mask:0xf bank_mask:0xf
	v_cndmask_b32_dpp v41, v39, v41, vcc quad_perm:[2,3,0,1] row_mask:0xf bank_mask:0xf
	v_cndmask_b32_dpp v24, v22, v24, vcc quad_perm:[2,3,0,1] row_mask:0xf bank_mask:0xf
	v_cndmask_b32_dpp v25, v23, v25, vcc quad_perm:[2,3,0,1] row_mask:0xf bank_mask:0xf
	s_mov_b32 vcc_lo, 0x33333333
	s_mov_b32 vcc_hi, 0x33333333
	s_nop 1
	v_cndmask_b32_dpp v38, v82, v38, vcc quad_perm:[2,3,0,1] row_mask:0xf bank_mask:0xf
	v_cndmask_b32_dpp v39, v83, v39, vcc quad_perm:[2,3,0,1] row_mask:0xf bank_mask:0xf
	v_cndmask_b32_dpp v22, v254, v22, vcc quad_perm:[2,3,0,1] row_mask:0xf bank_mask:0xf
	v_cndmask_b32_dpp v23, v255, v23, vcc quad_perm:[2,3,0,1] row_mask:0xf bank_mask:0xf
	v_cvt_pk_bf16_f32 v38, v38, v39
	v_cvt_pk_bf16_f32 v39, v40, v41
	v_cvt_pk_bf16_f32 v22, v22, v23
	v_cvt_pk_bf16_f32 v23, v24, v25
	global_store_dwordx2 v[252:253], v[38:39], off offset:128
	global_store_dwordx2 v[252:253], v[22:23], off offset:192
	s_mov_b32 s100, 0x8000
	v_lshl_add_u64 v[252:253], v[250:251], 0, s[100:101]
	v_mul_f32_e32 v10, v10, v74
	v_mul_f32_e32 v11, v11, v75
	v_mul_f32_e32 v12, v12, v76
	v_mul_f32_e32 v13, v13, v77
	v_mul_f32_e32 v58, v58, v74
	v_mul_f32_e32 v59, v59, v75
	v_mul_f32_e32 v60, v60, v76
	v_mul_f32_e32 v61, v61, v77
	s_mov_b32 vcc_lo, 0xaaaaaaaa
	s_mov_b32 vcc_hi, 0xaaaaaaaa
	s_nop 1
	v_mov_b32_e32 v82, v11
	v_mov_b32_e32 v83, v13
	v_mov_b32_e32 v254, v59
	v_mov_b32_e32 v255, v61
	v_cndmask_b32_dpp v11, v10, v11, vcc quad_perm:[1,0,3,2] row_mask:0xf bank_mask:0xf
	v_cndmask_b32_dpp v13, v12, v13, vcc quad_perm:[1,0,3,2] row_mask:0xf bank_mask:0xf
	v_cndmask_b32_dpp v59, v58, v59, vcc quad_perm:[1,0,3,2] row_mask:0xf bank_mask:0xf
	v_cndmask_b32_dpp v61, v60, v61, vcc quad_perm:[1,0,3,2] row_mask:0xf bank_mask:0xf
	s_mov_b32 vcc_lo, 0x55555555
	s_mov_b32 vcc_hi, 0x55555555
	s_nop 1
	v_cndmask_b32_dpp v10, v82, v10, vcc quad_perm:[1,0,3,2] row_mask:0xf bank_mask:0xf
	v_cndmask_b32_dpp v12, v83, v12, vcc quad_perm:[1,0,3,2] row_mask:0xf bank_mask:0xf
	v_cndmask_b32_dpp v58, v254, v58, vcc quad_perm:[1,0,3,2] row_mask:0xf bank_mask:0xf
; __device__ __forceinline__ bf16_t f2bf(float f) { return (bf16_t)(cvt_pk_bf16(f, 0.f) & 0xffffu); }
; __device__ __forceinline__ int crow(int r, int hi) { return (r & 3) + 8 * (r >> 2) + 4 * hi; }
; __device__ __forceinline__ void attn_dense_body(const bf16_t* __restrict__ Qb, const bf16_t* __restrict__ Kh, const bf16_t* __restrict__ Vh, bf16_t* __restrict__ Ob, int seq, char* lds) {
;     ...
;   bf16_t* Ow = Ob + (long)(wid * QBLK) * LDO;
; #pragma unroll
;   for (int r = 0; r < 16; ++r) { int orow = crow(r, hi);
;     for (int d0 = 0; d0 < 4; ++d0) Ow[(long)orow * LDO + d0 * 32 + r32] = f2bf(o[d0][r] * rli[r]); }
	v_cndmask_b32_dpp v60, v255, v60, vcc quad_perm:[1,0,3,2] row_mask:0xf bank_mask:0xf
	s_mov_b32 vcc_lo, 0xcccccccc
	s_mov_b32 vcc_hi, 0xcccccccc
	s_nop 1
	v_mov_b32_e32 v82, v12
	v_mov_b32_e32 v83, v13
	v_mov_b32_e32 v254, v60
	v_mov_b32_e32 v255, v61
	v_cndmask_b32_dpp v12, v10, v12, vcc quad_perm:[2,3,0,1] row_mask:0xf bank_mask:0xf
	v_cndmask_b32_dpp v13, v11, v13, vcc quad_perm:[2,3,0,1] row_mask:0xf bank_mask:0xf
	v_cndmask_b32_dpp v60, v58, v60, vcc quad_perm:[2,3,0,1] row_mask:0xf bank_mask:0xf
	v_cndmask_b32_dpp v61, v59, v61, vcc quad_perm:[2,3,0,1] row_mask:0xf bank_mask:0xf
	s_mov_b32 vcc_lo, 0x33333333
	s_mov_b32 vcc_hi, 0x33333333
	s_nop 1
	v_cndmask_b32_dpp v10, v82, v10, vcc quad_perm:[2,3,0,1] row_mask:0xf bank_mask:0xf
	v_cndmask_b32_dpp v11, v83, v11, vcc quad_perm:[2,3,0,1] row_mask:0xf bank_mask:0xf
	v_cndmask_b32_dpp v58, v254, v58, vcc quad_perm:[2,3,0,1] row_mask:0xf bank_mask:0xf
	v_cndmask_b32_dpp v59, v255, v59, vcc quad_perm:[2,3,0,1] row_mask:0xf bank_mask:0xf
	v_cvt_pk_bf16_f32 v10, v10, v11
	v_cvt_pk_bf16_f32 v11, v12, v13
	v_cvt_pk_bf16_f32 v58, v58, v59
	v_cvt_pk_bf16_f32 v59, v60, v61
	global_store_dwordx2 v[252:253], v[10:11], off
	global_store_dwordx2 v[252:253], v[58:59], off offset:64
	v_mul_f32_e32 v42, v42, v74
	v_mul_f32_e32 v43, v43, v75
	v_mul_f32_e32 v44, v44, v76
	v_mul_f32_e32 v45, v45, v77
	v_mul_f32_e32 v26, v26, v74
	v_mul_f32_e32 v27, v27, v75
	v_mul_f32_e32 v28, v28, v76
	v_mul_f32_e32 v29, v29, v77
	s_mov_b32 vcc_lo, 0xaaaaaaaa
	s_mov_b32 vcc_hi, 0xaaaaaaaa
	s_nop 1
	v_mov_b32_e32 v82, v43
	v_mov_b32_e32 v83, v45
	v_mov_b32_e32 v254, v27
	v_mov_b32_e32 v255, v29
	v_cndmask_b32_dpp v43, v42, v43, vcc quad_perm:[1,0,3,2] row_mask:0xf bank_mask:0xf
	v_cndmask_b32_dpp v45, v44, v45, vcc quad_perm:[1,0,3,2] row_mask:0xf bank_mask:0xf
	v_cndmask_b32_dpp v27, v26, v27, vcc quad_perm:[1,0,3,2] row_mask:0xf bank_mask:0xf
	v_cndmask_b32_dpp v29, v28, v29, vcc quad_perm:[1,0,3,2] row_mask:0xf bank_mask:0xf
	s_mov_b32 vcc_lo, 0x55555555
	s_mov_b32 vcc_hi, 0x55555555
	s_nop 1
	v_cndmask_b32_dpp v42, v82, v42, vcc quad_perm:[1,0,3,2] row_mask:0xf bank_mask:0xf
	v_cndmask_b32_dpp v44, v83, v44, vcc quad_perm:[1,0,3,2] row_mask:0xf bank_mask:0xf
	v_cndmask_b32_dpp v26, v254, v26, vcc quad_perm:[1,0,3,2] row_mask:0xf bank_mask:0xf
	v_cndmask_b32_dpp v28, v255, v28, vcc quad_perm:[1,0,3,2] row_mask:0xf bank_mask:0xf
	s_mov_b32 vcc_lo, 0xcccccccc
	s_mov_b32 vcc_hi, 0xcccccccc
	s_nop 1
	v_mov_b32_e32 v82, v44
	v_mov_b32_e32 v83, v45
	v_mov_b32_e32 v254, v28
	v_mov_b32_e32 v255, v29
	v_cndmask_b32_dpp v44, v42, v44, vcc quad_perm:[2,3,0,1] row_mask:0xf bank_mask:0xf
	v_cndmask_b32_dpp v45, v43, v45, vcc quad_perm:[2,3,0,1] row_mask:0xf bank_mask:0xf
	v_cndmask_b32_dpp v28, v26, v28, vcc quad_perm:[2,3,0,1] row_mask:0xf bank_mask:0xf
	v_cndmask_b32_dpp v29, v27, v29, vcc quad_perm:[2,3,0,1] row_mask:0xf bank_mask:0xf
	s_mov_b32 vcc_lo, 0x33333333
	s_mov_b32 vcc_hi, 0x33333333
	s_nop 1
	v_cndmask_b32_dpp v42, v82, v42, vcc quad_perm:[2,3,0,1] row_mask:0xf bank_mask:0xf
	v_cndmask_b32_dpp v43, v83, v43, vcc quad_perm:[2,3,0,1] row_mask:0xf bank_mask:0xf
	v_cndmask_b32_dpp v26, v254, v26, vcc quad_perm:[2,3,0,1] row_mask:0xf bank_mask:0xf
	v_cndmask_b32_dpp v27, v255, v27, vcc quad_perm:[2,3,0,1] row_mask:0xf bank_mask:0xf
	v_cvt_pk_bf16_f32 v42, v42, v43
	v_cvt_pk_bf16_f32 v43, v44, v45
	v_cvt_pk_bf16_f32 v26, v26, v27
	v_cvt_pk_bf16_f32 v27, v28, v29
	global_store_dwordx2 v[252:253], v[42:43], off offset:128
	global_store_dwordx2 v[252:253], v[26:27], off offset:192
	s_mov_b32 s100, 0xc000
	v_lshl_add_u64 v[252:253], v[250:251], 0, s[100:101]
	v_mul_f32_e32 v14, v14, v78
	v_mul_f32_e32 v15, v15, v79
	v_mul_f32_e32 v16, v16, v80
	v_mul_f32_e32 v17, v17, v81
	v_mul_f32_e32 v62, v62, v78
	v_mul_f32_e32 v63, v63, v79
	v_mul_f32_e32 v64, v64, v80
	v_mul_f32_e32 v65, v65, v81
	s_mov_b32 vcc_lo, 0xaaaaaaaa
	s_mov_b32 vcc_hi, 0xaaaaaaaa
	s_nop 1
	v_mov_b32_e32 v82, v15
	v_mov_b32_e32 v83, v17
	v_mov_b32_e32 v254, v63
	v_mov_b32_e32 v255, v65
	v_cndmask_b32_dpp v15, v14, v15, vcc quad_perm:[1,0,3,2] row_mask:0xf bank_mask:0xf
	v_cndmask_b32_dpp v17, v16, v17, vcc quad_perm:[1,0,3,2] row_mask:0xf bank_mask:0xf
; __device__ __forceinline__ bf16_t f2bf(float f) { return (bf16_t)(cvt_pk_bf16(f, 0.f) & 0xffffu); }
; __device__ __forceinline__ int crow(int r, int hi) { return (r & 3) + 8 * (r >> 2) + 4 * hi; }
; __device__ __forceinline__ void attn_dense_body(const bf16_t* __restrict__ Qb, const bf16_t* __restrict__ Kh, const bf16_t* __restrict__ Vh, bf16_t* __restrict__ Ob, int seq, char* lds) {
;     ...
;   bf16_t* Ow = Ob + (long)(wid * QBLK) * LDO;
; #pragma unroll
;   for (int r = 0; r < 16; ++r) { int orow = crow(r, hi);
;     for (int d0 = 0; d0 < 4; ++d0) Ow[(long)orow * LDO + d0 * 32 + r32] = f2bf(o[d0][r] * rli[r]); }
;   __syncthreads();
	v_cndmask_b32_dpp v63, v62, v63, vcc quad_perm:[1,0,3,2] row_mask:0xf bank_mask:0xf
	v_cndmask_b32_dpp v65, v64, v65, vcc quad_perm:[1,0,3,2] row_mask:0xf bank_mask:0xf
	s_mov_b32 vcc_lo, 0x55555555
	s_mov_b32 vcc_hi, 0x55555555
	s_nop 1
	v_cndmask_b32_dpp v14, v82, v14, vcc quad_perm:[1,0,3,2] row_mask:0xf bank_mask:0xf
	v_cndmask_b32_dpp v16, v83, v16, vcc quad_perm:[1,0,3,2] row_mask:0xf bank_mask:0xf
	v_cndmask_b32_dpp v62, v254, v62, vcc quad_perm:[1,0,3,2] row_mask:0xf bank_mask:0xf
	v_cndmask_b32_dpp v64, v255, v64, vcc quad_perm:[1,0,3,2] row_mask:0xf bank_mask:0xf
	s_mov_b32 vcc_lo, 0xcccccccc
	s_mov_b32 vcc_hi, 0xcccccccc
	s_nop 1
	v_mov_b32_e32 v82, v16
	v_mov_b32_e32 v83, v17
	v_mov_b32_e32 v254, v64
	v_mov_b32_e32 v255, v65
	v_cndmask_b32_dpp v16, v14, v16, vcc quad_perm:[2,3,0,1] row_mask:0xf bank_mask:0xf
	v_cndmask_b32_dpp v17, v15, v17, vcc quad_perm:[2,3,0,1] row_mask:0xf bank_mask:0xf
	v_cndmask_b32_dpp v64, v62, v64, vcc quad_perm:[2,3,0,1] row_mask:0xf bank_mask:0xf
	v_cndmask_b32_dpp v65, v63, v65, vcc quad_perm:[2,3,0,1] row_mask:0xf bank_mask:0xf
	s_mov_b32 vcc_lo, 0x33333333
	s_mov_b32 vcc_hi, 0x33333333
	s_nop 1
	v_cndmask_b32_dpp v14, v82, v14, vcc quad_perm:[2,3,0,1] row_mask:0xf bank_mask:0xf
	v_cndmask_b32_dpp v15, v83, v15, vcc quad_perm:[2,3,0,1] row_mask:0xf bank_mask:0xf
	v_cndmask_b32_dpp v62, v254, v62, vcc quad_perm:[2,3,0,1] row_mask:0xf bank_mask:0xf
	v_cndmask_b32_dpp v63, v255, v63, vcc quad_perm:[2,3,0,1] row_mask:0xf bank_mask:0xf
	v_cvt_pk_bf16_f32 v14, v14, v15
	v_cvt_pk_bf16_f32 v15, v16, v17
	v_cvt_pk_bf16_f32 v62, v62, v63
	v_cvt_pk_bf16_f32 v63, v64, v65
	global_store_dwordx2 v[252:253], v[14:15], off
	global_store_dwordx2 v[252:253], v[62:63], off offset:64
	v_mul_f32_e32 v46, v46, v78
	v_mul_f32_e32 v47, v47, v79
	v_mul_f32_e32 v48, v48, v80
	v_mul_f32_e32 v49, v49, v81
	v_mul_f32_e32 v30, v30, v78
	v_mul_f32_e32 v31, v31, v79
	v_mul_f32_e32 v32, v32, v80
	v_mul_f32_e32 v33, v33, v81
	s_mov_b32 vcc_lo, 0xaaaaaaaa
	s_mov_b32 vcc_hi, 0xaaaaaaaa
	s_nop 1
	v_mov_b32_e32 v82, v47
	v_mov_b32_e32 v83, v49
	v_mov_b32_e32 v254, v31
	v_mov_b32_e32 v255, v33
	v_cndmask_b32_dpp v47, v46, v47, vcc quad_perm:[1,0,3,2] row_mask:0xf bank_mask:0xf
	v_cndmask_b32_dpp v49, v48, v49, vcc quad_perm:[1,0,3,2] row_mask:0xf bank_mask:0xf
	v_cndmask_b32_dpp v31, v30, v31, vcc quad_perm:[1,0,3,2] row_mask:0xf bank_mask:0xf
	v_cndmask_b32_dpp v33, v32, v33, vcc quad_perm:[1,0,3,2] row_mask:0xf bank_mask:0xf
	s_mov_b32 vcc_lo, 0x55555555
	s_mov_b32 vcc_hi, 0x55555555
	s_nop 1
	v_cndmask_b32_dpp v46, v82, v46, vcc quad_perm:[1,0,3,2] row_mask:0xf bank_mask:0xf
	v_cndmask_b32_dpp v48, v83, v48, vcc quad_perm:[1,0,3,2] row_mask:0xf bank_mask:0xf
	v_cndmask_b32_dpp v30, v254, v30, vcc quad_perm:[1,0,3,2] row_mask:0xf bank_mask:0xf
	v_cndmask_b32_dpp v32, v255, v32, vcc quad_perm:[1,0,3,2] row_mask:0xf bank_mask:0xf
	s_mov_b32 vcc_lo, 0xcccccccc
	s_mov_b32 vcc_hi, 0xcccccccc
	s_nop 1
	v_mov_b32_e32 v82, v48
	v_mov_b32_e32 v83, v49
	v_mov_b32_e32 v254, v32
	v_mov_b32_e32 v255, v33
	v_cndmask_b32_dpp v48, v46, v48, vcc quad_perm:[2,3,0,1] row_mask:0xf bank_mask:0xf
	v_cndmask_b32_dpp v49, v47, v49, vcc quad_perm:[2,3,0,1] row_mask:0xf bank_mask:0xf
	v_cndmask_b32_dpp v32, v30, v32, vcc quad_perm:[2,3,0,1] row_mask:0xf bank_mask:0xf
	v_cndmask_b32_dpp v33, v31, v33, vcc quad_perm:[2,3,0,1] row_mask:0xf bank_mask:0xf
	s_mov_b32 vcc_lo, 0x33333333
	s_mov_b32 vcc_hi, 0x33333333
	s_nop 1
	v_cndmask_b32_dpp v46, v82, v46, vcc quad_perm:[2,3,0,1] row_mask:0xf bank_mask:0xf
	v_cndmask_b32_dpp v47, v83, v47, vcc quad_perm:[2,3,0,1] row_mask:0xf bank_mask:0xf
	v_cndmask_b32_dpp v30, v254, v30, vcc quad_perm:[2,3,0,1] row_mask:0xf bank_mask:0xf
	v_cndmask_b32_dpp v31, v255, v31, vcc quad_perm:[2,3,0,1] row_mask:0xf bank_mask:0xf
	v_cvt_pk_bf16_f32 v46, v46, v47
	v_cvt_pk_bf16_f32 v47, v48, v49
	v_cvt_pk_bf16_f32 v30, v30, v31
	v_cvt_pk_bf16_f32 v31, v32, v33
	global_store_dwordx2 v[252:253], v[46:47], off offset:128
	global_store_dwordx2 v[252:253], v[30:31], off offset:192
	s_add_i32 s42, s42, s33
	s_cmpk_gt_i32 s42, 0xff
	s_waitcnt vmcnt(63) expcnt(7) lgkmcnt(15)
	s_barrier
	s_cbranch_scc1 .LBB0_729

; __device__ __forceinline__ bf16_t f2bf(float f) { return (bf16_t)(cvt_pk_bf16(f, 0.f) & 0xffffu); }
; __device__ __forceinline__ int crow(int r, int hi) { return (r & 3) + 8 * (r >> 2) + 4 * hi; }
; __device__ __forceinline__ void attn_dense_body(const bf16_t* __restrict__ Qb, const bf16_t* __restrict__ Kh, const bf16_t* __restrict__ Vh, bf16_t* __restrict__ Ob, int seq, char* lds) {
;     ...
;   if (hi == 0) li_l[r32] = l_reg; asm volatile("s_waitcnt lgkmcnt(0)" ::: "memory");
;   float rli[16];
; #pragma unroll
;   for (int r = 0; r < 16; ++r) rli[r] = __builtin_amdgcn_rcpf(li_l[crow(r, hi)]);
;   bf16_t* Ow = Ob + (long)(wid * QBLK) * LDO;
; #pragma unroll
;   for (int r = 0; r < 16; ++r) { int orow = crow(r, hi);
;     for (int d0 = 0; d0 < 4; ++d0) Ow[(long)orow * LDO + d0 * 32 + r32] = f2bf(o[d0][r] * rli[r]); }
.LBB0_1683:
	s_or_b64 exec, exec, s[4:5]
	s_waitcnt lgkmcnt(0)
	v_add_u32_e32 v82, v192, v180
	ds_read_b128 v[66:69], v82
	ds_read_b128 v[70:73], v82 offset:32
	ds_read_b128 v[74:77], v82 offset:64
	ds_read_b128 v[78:81], v82 offset:96
	s_mov_b32 s101, 0
	v_lshl_add_u64 v[250:251], s[66:67], 1, v[184:185]
	v_and_b32_e32 v248, 3, v0
	v_mul_u32_u24_e32 v248, 0x7fe, v248
	v_mov_b32_e32 v249, 0
	s_nop 0
	v_lshl_add_u64 v[250:251], v[248:249], 0, v[250:251]
	s_waitcnt lgkmcnt(0)
	v_rcp_f32_e32 v66, v66
	v_rcp_f32_e32 v67, v67
	v_rcp_f32_e32 v68, v68
	v_rcp_f32_e32 v69, v69
	v_rcp_f32_e32 v70, v70
	v_rcp_f32_e32 v71, v71
	v_rcp_f32_e32 v72, v72
	v_rcp_f32_e32 v73, v73
	v_rcp_f32_e32 v74, v74
	v_rcp_f32_e32 v75, v75
	v_rcp_f32_e32 v76, v76
	v_rcp_f32_e32 v77, v77
	v_rcp_f32_e32 v78, v78
	v_rcp_f32_e32 v79, v79
	v_rcp_f32_e32 v80, v80
	v_rcp_f32_e32 v81, v81
	v_mul_f32_e32 v2, v2, v66
	v_mul_f32_e32 v3, v3, v67
	v_mul_f32_e32 v4, v4, v68
	v_mul_f32_e32 v5, v5, v69
	v_mul_f32_e32 v50, v50, v66
	v_mul_f32_e32 v51, v51, v67
	v_mul_f32_e32 v52, v52, v68
	v_mul_f32_e32 v53, v53, v69
	s_mov_b32 vcc_lo, 0xaaaaaaaa
	s_mov_b32 vcc_hi, 0xaaaaaaaa
	s_nop 1
	v_mov_b32_e32 v82, v3
	v_mov_b32_e32 v83, v5
	v_mov_b32_e32 v254, v51
	v_mov_b32_e32 v255, v53
	v_cndmask_b32_dpp v3, v2, v3, vcc quad_perm:[1,0,3,2] row_mask:0xf bank_mask:0xf
	v_cndmask_b32_dpp v5, v4, v5, vcc quad_perm:[1,0,3,2] row_mask:0xf bank_mask:0xf
	v_cndmask_b32_dpp v51, v50, v51, vcc quad_perm:[1,0,3,2] row_mask:0xf bank_mask:0xf
	v_cndmask_b32_dpp v53, v52, v53, vcc quad_perm:[1,0,3,2] row_mask:0xf bank_mask:0xf
	s_mov_b32 vcc_lo, 0x55555555
	s_mov_b32 vcc_hi, 0x55555555
	s_nop 1
	v_cndmask_b32_dpp v2, v82, v2, vcc quad_perm:[1,0,3,2] row_mask:0xf bank_mask:0xf
	v_cndmask_b32_dpp v4, v83, v4, vcc quad_perm:[1,0,3,2] row_mask:0xf bank_mask:0xf
	v_cndmask_b32_dpp v50, v254, v50, vcc quad_perm:[1,0,3,2] row_mask:0xf bank_mask:0xf
	v_cndmask_b32_dpp v52, v255, v52, vcc quad_perm:[1,0,3,2] row_mask:0xf bank_mask:0xf
	s_mov_b32 vcc_lo, 0xcccccccc
	s_mov_b32 vcc_hi, 0xcccccccc
	s_nop 1
	v_mov_b32_e32 v82, v4
	v_mov_b32_e32 v83, v5
	v_mov_b32_e32 v254, v52
	v_mov_b32_e32 v255, v53
	v_cndmask_b32_dpp v4, v2, v4, vcc quad_perm:[2,3,0,1] row_mask:0xf bank_mask:0xf
	v_cndmask_b32_dpp v5, v3, v5, vcc quad_perm:[2,3,0,1] row_mask:0xf bank_mask:0xf
	v_cndmask_b32_dpp v52, v50, v52, vcc quad_perm:[2,3,0,1] row_mask:0xf bank_mask:0xf
	v_cndmask_b32_dpp v53, v51, v53, vcc quad_perm:[2,3,0,1] row_mask:0xf bank_mask:0xf
	s_mov_b32 vcc_lo, 0x33333333
	s_mov_b32 vcc_hi, 0x33333333
	s_nop 1
	v_cndmask_b32_dpp v2, v82, v2, vcc quad_perm:[2,3,0,1] row_mask:0xf bank_mask:0xf
	v_cndmask_b32_dpp v3, v83, v3, vcc quad_perm:[2,3,0,1] row_mask:0xf bank_mask:0xf
	v_cndmask_b32_dpp v50, v254, v50, vcc quad_perm:[2,3,0,1] row_mask:0xf bank_mask:0xf
	v_cndmask_b32_dpp v51, v255, v51, vcc quad_perm:[2,3,0,1] row_mask:0xf bank_mask:0xf
	v_cvt_pk_bf16_f32 v2, v2, v3
	v_cvt_pk_bf16_f32 v3, v4, v5
	v_cvt_pk_bf16_f32 v50, v50, v51
	v_cvt_pk_bf16_f32 v51, v52, v53
	global_store_dwordx2 v[250:251], v[2:3], off
	global_store_dwordx2 v[250:251], v[50:51], off offset:64
	v_mul_f32_e32 v34, v34, v66
	v_mul_f32_e32 v35, v35, v67
	v_mul_f32_e32 v36, v36, v68
	v_mul_f32_e32 v37, v37, v69
	v_mul_f32_e32 v18, v18, v66
	v_mul_f32_e32 v19, v19, v67
	v_mul_f32_e32 v20, v20, v68
	v_mul_f32_e32 v21, v21, v69
	s_mov_b32 vcc_lo, 0xaaaaaaaa
	s_mov_b32 vcc_hi, 0xaaaaaaaa
	s_nop 1
	v_mov_b32_e32 v82, v35
	v_mov_b32_e32 v83, v37
	v_mov_b32_e32 v254, v19
	v_mov_b32_e32 v255, v21
	v_cndmask_b32_dpp v35, v34, v35, vcc quad_perm:[1,0,3,2] row_mask:0xf bank_mask:0xf
	v_cndmask_b32_dpp v37, v36, v37, vcc quad_perm:[1,0,3,2] row_mask:0xf bank_mask:0xf
	v_cndmask_b32_dpp v19, v18, v19, vcc quad_perm:[1,0,3,2] row_mask:0xf bank_mask:0xf
	v_cndmask_b32_dpp v21, v20, v21, vcc quad_perm:[1,0,3,2] row_mask:0xf bank_mask:0xf
	s_mov_b32 vcc_lo, 0x55555555
	s_mov_b32 vcc_hi, 0x55555555
	s_nop 1
	v_cndmask_b32_dpp v34, v82, v34, vcc quad_perm:[1,0,3,2] row_mask:0xf bank_mask:0xf
	v_cndmask_b32_dpp v36, v83, v36, vcc quad_perm:[1,0,3,2] row_mask:0xf bank_mask:0xf
	v_cndmask_b32_dpp v18, v254, v18, vcc quad_perm:[1,0,3,2] row_mask:0xf bank_mask:0xf
	v_cndmask_b32_dpp v20, v255, v20, vcc quad_perm:[1,0,3,2] row_mask:0xf bank_mask:0xf
	s_mov_b32 vcc_lo, 0xcccccccc
	s_mov_b32 vcc_hi, 0xcccccccc
	s_nop 1
	v_mov_b32_e32 v82, v36
	v_mov_b32_e32 v83, v37
	v_mov_b32_e32 v254, v20
	v_mov_b32_e32 v255, v21
	v_cndmask_b32_dpp v36, v34, v36, vcc quad_perm:[2,3,0,1] row_mask:0xf bank_mask:0xf
	v_cndmask_b32_dpp v37, v35, v37, vcc quad_perm:[2,3,0,1] row_mask:0xf bank_mask:0xf
	v_cndmask_b32_dpp v20, v18, v20, vcc quad_perm:[2,3,0,1] row_mask:0xf bank_mask:0xf
	v_cndmask_b32_dpp v21, v19, v21, vcc quad_perm:[2,3,0,1] row_mask:0xf bank_mask:0xf
	s_mov_b32 vcc_lo, 0x33333333
	s_mov_b32 vcc_hi, 0x33333333
	s_nop 1
	v_cndmask_b32_dpp v34, v82, v34, vcc quad_perm:[2,3,0,1] row_mask:0xf bank_mask:0xf
	v_cndmask_b32_dpp v35, v83, v35, vcc quad_perm:[2,3,0,1] row_mask:0xf bank_mask:0xf
	v_cndmask_b32_dpp v18, v254, v18, vcc quad_perm:[2,3,0,1] row_mask:0xf bank_mask:0xf
	v_cndmask_b32_dpp v19, v255, v19, vcc quad_perm:[2,3,0,1] row_mask:0xf bank_mask:0xf
	v_cvt_pk_bf16_f32 v34, v34, v35
	v_cvt_pk_bf16_f32 v35, v36, v37
	v_cvt_pk_bf16_f32 v18, v18, v19
	v_cvt_pk_bf16_f32 v19, v20, v21
	global_store_dwordx2 v[250:251], v[34:35], off offset:128
	global_store_dwordx2 v[250:251], v[18:19], off offset:192
	s_mov_b32 s100, 0x4000
	v_lshl_add_u64 v[252:253], v[250:251], 0, s[100:101]
	v_mul_f32_e32 v6, v6, v70
	v_mul_f32_e32 v7, v7, v71
	v_mul_f32_e32 v8, v8, v72
	v_mul_f32_e32 v9, v9, v73
; __device__ __forceinline__ bf16_t f2bf(float f) { return (bf16_t)(cvt_pk_bf16(f, 0.f) & 0xffffu); }
; __device__ __forceinline__ int crow(int r, int hi) { return (r & 3) + 8 * (r >> 2) + 4 * hi; }
; __device__ __forceinline__ void attn_dense_body(const bf16_t* __restrict__ Qb, const bf16_t* __restrict__ Kh, const bf16_t* __restrict__ Vh, bf16_t* __restrict__ Ob, int seq, char* lds) {
;     ...
;   bf16_t* Ow = Ob + (long)(wid * QBLK) * LDO;
; #pragma unroll
;   for (int r = 0; r < 16; ++r) { int orow = crow(r, hi);
;     for (int d0 = 0; d0 < 4; ++d0) Ow[(long)orow * LDO + d0 * 32 + r32] = f2bf(o[d0][r] * rli[r]); }
	v_mul_f32_e32 v54, v54, v70
	v_mul_f32_e32 v55, v55, v71
	v_mul_f32_e32 v56, v56, v72
	v_mul_f32_e32 v57, v57, v73
	s_mov_b32 vcc_lo, 0xaaaaaaaa
	s_mov_b32 vcc_hi, 0xaaaaaaaa
	s_nop 1
	v_mov_b32_e32 v82, v7
	v_mov_b32_e32 v83, v9
	v_mov_b32_e32 v254, v55
	v_mov_b32_e32 v255, v57
	v_cndmask_b32_dpp v7, v6, v7, vcc quad_perm:[1,0,3,2] row_mask:0xf bank_mask:0xf
	v_cndmask_b32_dpp v9, v8, v9, vcc quad_perm:[1,0,3,2] row_mask:0xf bank_mask:0xf
	v_cndmask_b32_dpp v55, v54, v55, vcc quad_perm:[1,0,3,2] row_mask:0xf bank_mask:0xf
	v_cndmask_b32_dpp v57, v56, v57, vcc quad_perm:[1,0,3,2] row_mask:0xf bank_mask:0xf
	s_mov_b32 vcc_lo, 0x55555555
	s_mov_b32 vcc_hi, 0x55555555
	s_nop 1
	v_cndmask_b32_dpp v6, v82, v6, vcc quad_perm:[1,0,3,2] row_mask:0xf bank_mask:0xf
	v_cndmask_b32_dpp v8, v83, v8, vcc quad_perm:[1,0,3,2] row_mask:0xf bank_mask:0xf
	v_cndmask_b32_dpp v54, v254, v54, vcc quad_perm:[1,0,3,2] row_mask:0xf bank_mask:0xf
	v_cndmask_b32_dpp v56, v255, v56, vcc quad_perm:[1,0,3,2] row_mask:0xf bank_mask:0xf
	s_mov_b32 vcc_lo, 0xcccccccc
	s_mov_b32 vcc_hi, 0xcccccccc
	s_nop 1
	v_mov_b32_e32 v82, v8
	v_mov_b32_e32 v83, v9
	v_mov_b32_e32 v254, v56
	v_mov_b32_e32 v255, v57
	v_cndmask_b32_dpp v8, v6, v8, vcc quad_perm:[2,3,0,1] row_mask:0xf bank_mask:0xf
	v_cndmask_b32_dpp v9, v7, v9, vcc quad_perm:[2,3,0,1] row_mask:0xf bank_mask:0xf
	v_cndmask_b32_dpp v56, v54, v56, vcc quad_perm:[2,3,0,1] row_mask:0xf bank_mask:0xf
	v_cndmask_b32_dpp v57, v55, v57, vcc quad_perm:[2,3,0,1] row_mask:0xf bank_mask:0xf
	s_mov_b32 vcc_lo, 0x33333333
	s_mov_b32 vcc_hi, 0x33333333
	s_nop 1
	v_cndmask_b32_dpp v6, v82, v6, vcc quad_perm:[2,3,0,1] row_mask:0xf bank_mask:0xf
	v_cndmask_b32_dpp v7, v83, v7, vcc quad_perm:[2,3,0,1] row_mask:0xf bank_mask:0xf
	v_cndmask_b32_dpp v54, v254, v54, vcc quad_perm:[2,3,0,1] row_mask:0xf bank_mask:0xf
	v_cndmask_b32_dpp v55, v255, v55, vcc quad_perm:[2,3,0,1] row_mask:0xf bank_mask:0xf
	v_cvt_pk_bf16_f32 v6, v6, v7
	v_cvt_pk_bf16_f32 v7, v8, v9
	v_cvt_pk_bf16_f32 v54, v54, v55
	v_cvt_pk_bf16_f32 v55, v56, v57
	global_store_dwordx2 v[252:253], v[6:7], off
	global_store_dwordx2 v[252:253], v[54:55], off offset:64
	v_mul_f32_e32 v38, v38, v70
	v_mul_f32_e32 v39, v39, v71
	v_mul_f32_e32 v40, v40, v72
	v_mul_f32_e32 v41, v41, v73
	v_mul_f32_e32 v22, v22, v70
	v_mul_f32_e32 v23, v23, v71
	v_mul_f32_e32 v24, v24, v72
	v_mul_f32_e32 v25, v25, v73
	s_mov_b32 vcc_lo, 0xaaaaaaaa
	s_mov_b32 vcc_hi, 0xaaaaaaaa
	s_nop 1
	v_mov_b32_e32 v82, v39
	v_mov_b32_e32 v83, v41
	v_mov_b32_e32 v254, v23
	v_mov_b32_e32 v255, v25
	v_cndmask_b32_dpp v39, v38, v39, vcc quad_perm:[1,0,3,2] row_mask:0xf bank_mask:0xf
	v_cndmask_b32_dpp v41, v40, v41, vcc quad_perm:[1,0,3,2] row_mask:0xf bank_mask:0xf
	v_cndmask_b32_dpp v23, v22, v23, vcc quad_perm:[1,0,3,2] row_mask:0xf bank_mask:0xf
	v_cndmask_b32_dpp v25, v24, v25, vcc quad_perm:[1,0,3,2] row_mask:0xf bank_mask:0xf
	s_mov_b32 vcc_lo, 0x55555555
	s_mov_b32 vcc_hi, 0x55555555
	s_nop 1
	v_cndmask_b32_dpp v38, v82, v38, vcc quad_perm:[1,0,3,2] row_mask:0xf bank_mask:0xf
	v_cndmask_b32_dpp v40, v83, v40, vcc quad_perm:[1,0,3,2] row_mask:0xf bank_mask:0xf
	v_cndmask_b32_dpp v22, v254, v22, vcc quad_perm:[1,0,3,2] row_mask:0xf bank_mask:0xf
	v_cndmask_b32_dpp v24, v255, v24, vcc quad_perm:[1,0,3,2] row_mask:0xf bank_mask:0xf
	s_mov_b32 vcc_lo, 0xcccccccc
	s_mov_b32 vcc_hi, 0xcccccccc
	s_nop 1
	v_mov_b32_e32 v82, v40
	v_mov_b32_e32 v83, v41
	v_mov_b32_e32 v254, v24
	v_mov_b32_e32 v255, v25
	v_cndmask_b32_dpp v40, v38, v40, vcc quad_perm:[2,3,0,1] row_mask:0xf bank_mask:0xf
	v_cndmask_b32_dpp v41, v39, v41, vcc quad_perm:[2,3,0,1] row_mask:0xf bank_mask:0xf
	v_cndmask_b32_dpp v24, v22, v24, vcc quad_perm:[2,3,0,1] row_mask:0xf bank_mask:0xf
	v_cndmask_b32_dpp v25, v23, v25, vcc quad_perm:[2,3,0,1] row_mask:0xf bank_mask:0xf
	s_mov_b32 vcc_lo, 0x33333333
	s_mov_b32 vcc_hi, 0x33333333
	s_nop 1
	v_cndmask_b32_dpp v38, v82, v38, vcc quad_perm:[2,3,0,1] row_mask:0xf bank_mask:0xf
	v_cndmask_b32_dpp v39, v83, v39, vcc quad_perm:[2,3,0,1] row_mask:0xf bank_mask:0xf
	v_cndmask_b32_dpp v22, v254, v22, vcc quad_perm:[2,3,0,1] row_mask:0xf bank_mask:0xf
	v_cndmask_b32_dpp v23, v255, v23, vcc quad_perm:[2,3,0,1] row_mask:0xf bank_mask:0xf
	v_cvt_pk_bf16_f32 v38, v38, v39
	v_cvt_pk_bf16_f32 v39, v40, v41
	v_cvt_pk_bf16_f32 v22, v22, v23
	v_cvt_pk_bf16_f32 v23, v24, v25
	global_store_dwordx2 v[252:253], v[38:39], off offset:128
	global_store_dwordx2 v[252:253], v[22:23], off offset:192
	s_mov_b32 s100, 0x8000
	v_lshl_add_u64 v[252:253], v[250:251], 0, s[100:101]
	v_mul_f32_e32 v10, v10, v74
	v_mul_f32_e32 v11, v11, v75
	v_mul_f32_e32 v12, v12, v76
	v_mul_f32_e32 v13, v13, v77
	v_mul_f32_e32 v58, v58, v74
	v_mul_f32_e32 v59, v59, v75
	v_mul_f32_e32 v60, v60, v76
	v_mul_f32_e32 v61, v61, v77
	s_mov_b32 vcc_lo, 0xaaaaaaaa
	s_mov_b32 vcc_hi, 0xaaaaaaaa
	s_nop 1
	v_mov_b32_e32 v82, v11
	v_mov_b32_e32 v83, v13
	v_mov_b32_e32 v254, v59
	v_mov_b32_e32 v255, v61
	v_cndmask_b32_dpp v11, v10, v11, vcc quad_perm:[1,0,3,2] row_mask:0xf bank_mask:0xf
	v_cndmask_b32_dpp v13, v12, v13, vcc quad_perm:[1,0,3,2] row_mask:0xf bank_mask:0xf
	v_cndmask_b32_dpp v59, v58, v59, vcc quad_perm:[1,0,3,2] row_mask:0xf bank_mask:0xf
	v_cndmask_b32_dpp v61, v60, v61, vcc quad_perm:[1,0,3,2] row_mask:0xf bank_mask:0xf
	s_mov_b32 vcc_lo, 0x55555555
	s_mov_b32 vcc_hi, 0x55555555
	s_nop 1
	v_cndmask_b32_dpp v10, v82, v10, vcc quad_perm:[1,0,3,2] row_mask:0xf bank_mask:0xf
	v_cndmask_b32_dpp v12, v83, v12, vcc quad_perm:[1,0,3,2] row_mask:0xf bank_mask:0xf
	v_cndmask_b32_dpp v58, v254, v58, vcc quad_perm:[1,0,3,2] row_mask:0xf bank_mask:0xf
; __device__ __forceinline__ bf16_t f2bf(float f) { return (bf16_t)(cvt_pk_bf16(f, 0.f) & 0xffffu); }
; __device__ __forceinline__ int crow(int r, int hi) { return (r & 3) + 8 * (r >> 2) + 4 * hi; }
; __device__ __forceinline__ void attn_dense_body(const bf16_t* __restrict__ Qb, const bf16_t* __restrict__ Kh, const bf16_t* __restrict__ Vh, bf16_t* __restrict__ Ob, int seq, char* lds) {
;     ...
;   bf16_t* Ow = Ob + (long)(wid * QBLK) * LDO;
; #pragma unroll
;   for (int r = 0; r < 16; ++r) { int orow = crow(r, hi);
;     for (int d0 = 0; d0 < 4; ++d0) Ow[(long)orow * LDO + d0 * 32 + r32] = f2bf(o[d0][r] * rli[r]); }
	v_cndmask_b32_dpp v60, v255, v60, vcc quad_perm:[1,0,3,2] row_mask:0xf bank_mask:0xf
	s_mov_b32 vcc_lo, 0xcccccccc
	s_mov_b32 vcc_hi, 0xcccccccc
	s_nop 1
	v_mov_b32_e32 v82, v12
	v_mov_b32_e32 v83, v13
	v_mov_b32_e32 v254, v60
	v_mov_b32_e32 v255, v61
	v_cndmask_b32_dpp v12, v10, v12, vcc quad_perm:[2,3,0,1] row_mask:0xf bank_mask:0xf
	v_cndmask_b32_dpp v13, v11, v13, vcc quad_perm:[2,3,0,1] row_mask:0xf bank_mask:0xf
	v_cndmask_b32_dpp v60, v58, v60, vcc quad_perm:[2,3,0,1] row_mask:0xf bank_mask:0xf
	v_cndmask_b32_dpp v61, v59, v61, vcc quad_perm:[2,3,0,1] row_mask:0xf bank_mask:0xf
	s_mov_b32 vcc_lo, 0x33333333
	s_mov_b32 vcc_hi, 0x33333333
	s_nop 1
	v_cndmask_b32_dpp v10, v82, v10, vcc quad_perm:[2,3,0,1] row_mask:0xf bank_mask:0xf
	v_cndmask_b32_dpp v11, v83, v11, vcc quad_perm:[2,3,0,1] row_mask:0xf bank_mask:0xf
	v_cndmask_b32_dpp v58, v254, v58, vcc quad_perm:[2,3,0,1] row_mask:0xf bank_mask:0xf
	v_cndmask_b32_dpp v59, v255, v59, vcc quad_perm:[2,3,0,1] row_mask:0xf bank_mask:0xf
	v_cvt_pk_bf16_f32 v10, v10, v11
	v_cvt_pk_bf16_f32 v11, v12, v13
	v_cvt_pk_bf16_f32 v58, v58, v59
	v_cvt_pk_bf16_f32 v59, v60, v61
	global_store_dwordx2 v[252:253], v[10:11], off
	global_store_dwordx2 v[252:253], v[58:59], off offset:64
	v_mul_f32_e32 v42, v42, v74
	v_mul_f32_e32 v43, v43, v75
	v_mul_f32_e32 v44, v44, v76
	v_mul_f32_e32 v45, v45, v77
	v_mul_f32_e32 v26, v26, v74
	v_mul_f32_e32 v27, v27, v75
	v_mul_f32_e32 v28, v28, v76
	v_mul_f32_e32 v29, v29, v77
	s_mov_b32 vcc_lo, 0xaaaaaaaa
	s_mov_b32 vcc_hi, 0xaaaaaaaa
	s_nop 1
	v_mov_b32_e32 v82, v43
	v_mov_b32_e32 v83, v45
	v_mov_b32_e32 v254, v27
	v_mov_b32_e32 v255, v29
	v_cndmask_b32_dpp v43, v42, v43, vcc quad_perm:[1,0,3,2] row_mask:0xf bank_mask:0xf
	v_cndmask_b32_dpp v45, v44, v45, vcc quad_perm:[1,0,3,2] row_mask:0xf bank_mask:0xf
	v_cndmask_b32_dpp v27, v26, v27, vcc quad_perm:[1,0,3,2] row_mask:0xf bank_mask:0xf
	v_cndmask_b32_dpp v29, v28, v29, vcc quad_perm:[1,0,3,2] row_mask:0xf bank_mask:0xf
	s_mov_b32 vcc_lo, 0x55555555
	s_mov_b32 vcc_hi, 0x55555555
	s_nop 1
	v_cndmask_b32_dpp v42, v82, v42, vcc quad_perm:[1,0,3,2] row_mask:0xf bank_mask:0xf
	v_cndmask_b32_dpp v44, v83, v44, vcc quad_perm:[1,0,3,2] row_mask:0xf bank_mask:0xf
	v_cndmask_b32_dpp v26, v254, v26, vcc quad_perm:[1,0,3,2] row_mask:0xf bank_mask:0xf
	v_cndmask_b32_dpp v28, v255, v28, vcc quad_perm:[1,0,3,2] row_mask:0xf bank_mask:0xf
	s_mov_b32 vcc_lo, 0xcccccccc
	s_mov_b32 vcc_hi, 0xcccccccc
	s_nop 1
	v_mov_b32_e32 v82, v44
	v_mov_b32_e32 v83, v45
	v_mov_b32_e32 v254, v28
	v_mov_b32_e32 v255, v29
	v_cndmask_b32_dpp v44, v42, v44, vcc quad_perm:[2,3,0,1] row_mask:0xf bank_mask:0xf
	v_cndmask_b32_dpp v45, v43, v45, vcc quad_perm:[2,3,0,1] row_mask:0xf bank_mask:0xf
	v_cndmask_b32_dpp v28, v26, v28, vcc quad_perm:[2,3,0,1] row_mask:0xf bank_mask:0xf
	v_cndmask_b32_dpp v29, v27, v29, vcc quad_perm:[2,3,0,1] row_mask:0xf bank_mask:0xf
	s_mov_b32 vcc_lo, 0x33333333
	s_mov_b32 vcc_hi, 0x33333333
	s_nop 1
	v_cndmask_b32_dpp v42, v82, v42, vcc quad_perm:[2,3,0,1] row_mask:0xf bank_mask:0xf
	v_cndmask_b32_dpp v43, v83, v43, vcc quad_perm:[2,3,0,1] row_mask:0xf bank_mask:0xf
	v_cndmask_b32_dpp v26, v254, v26, vcc quad_perm:[2,3,0,1] row_mask:0xf bank_mask:0xf
	v_cndmask_b32_dpp v27, v255, v27, vcc quad_perm:[2,3,0,1] row_mask:0xf bank_mask:0xf
	v_cvt_pk_bf16_f32 v42, v42, v43
	v_cvt_pk_bf16_f32 v43, v44, v45
	v_cvt_pk_bf16_f32 v26, v26, v27
	v_cvt_pk_bf16_f32 v27, v28, v29
	global_store_dwordx2 v[252:253], v[42:43], off offset:128
	global_store_dwordx2 v[252:253], v[26:27], off offset:192
	s_mov_b32 s100, 0xc000
	v_lshl_add_u64 v[252:253], v[250:251], 0, s[100:101]
	v_mul_f32_e32 v14, v14, v78
	v_mul_f32_e32 v15, v15, v79
	v_mul_f32_e32 v16, v16, v80
	v_mul_f32_e32 v17, v17, v81
	v_mul_f32_e32 v62, v62, v78
	v_mul_f32_e32 v63, v63, v79
	v_mul_f32_e32 v64, v64, v80
	v_mul_f32_e32 v65, v65, v81
	s_mov_b32 vcc_lo, 0xaaaaaaaa
	s_mov_b32 vcc_hi, 0xaaaaaaaa
	s_nop 1
	v_mov_b32_e32 v82, v15
	v_mov_b32_e32 v83, v17
	v_mov_b32_e32 v254, v63
	v_mov_b32_e32 v255, v65
	v_cndmask_b32_dpp v15, v14, v15, vcc quad_perm:[1,0,3,2] row_mask:0xf bank_mask:0xf
	v_cndmask_b32_dpp v17, v16, v17, vcc quad_perm:[1,0,3,2] row_mask:0xf bank_mask:0xf
; __device__ __forceinline__ bf16_t f2bf(float f) { return (bf16_t)(cvt_pk_bf16(f, 0.f) & 0xffffu); }
; __device__ __forceinline__ int crow(int r, int hi) { return (r & 3) + 8 * (r >> 2) + 4 * hi; }
; __device__ __forceinline__ void attn_dense_body(const bf16_t* __restrict__ Qb, const bf16_t* __restrict__ Kh, const bf16_t* __restrict__ Vh, bf16_t* __restrict__ Ob, int seq, char* lds) {
;     ...
;   bf16_t* Ow = Ob + (long)(wid * QBLK) * LDO;
; #pragma unroll
;   for (int r = 0; r < 16; ++r) { int orow = crow(r, hi);
;     for (int d0 = 0; d0 < 4; ++d0) Ow[(long)orow * LDO + d0 * 32 + r32] = f2bf(o[d0][r] * rli[r]); }
;   __syncthreads();
	v_cndmask_b32_dpp v63, v62, v63, vcc quad_perm:[1,0,3,2] row_mask:0xf bank_mask:0xf
	v_cndmask_b32_dpp v65, v64, v65, vcc quad_perm:[1,0,3,2] row_mask:0xf bank_mask:0xf
	s_mov_b32 vcc_lo, 0x55555555
	s_mov_b32 vcc_hi, 0x55555555
	s_nop 1
	v_cndmask_b32_dpp v14, v82, v14, vcc quad_perm:[1,0,3,2] row_mask:0xf bank_mask:0xf
	v_cndmask_b32_dpp v16, v83, v16, vcc quad_perm:[1,0,3,2] row_mask:0xf bank_mask:0xf
	v_cndmask_b32_dpp v62, v254, v62, vcc quad_perm:[1,0,3,2] row_mask:0xf bank_mask:0xf
	v_cndmask_b32_dpp v64, v255, v64, vcc quad_perm:[1,0,3,2] row_mask:0xf bank_mask:0xf
	s_mov_b32 vcc_lo, 0xcccccccc
	s_mov_b32 vcc_hi, 0xcccccccc
	s_nop 1
	v_mov_b32_e32 v82, v16
	v_mov_b32_e32 v83, v17
	v_mov_b32_e32 v254, v64
	v_mov_b32_e32 v255, v65
	v_cndmask_b32_dpp v16, v14, v16, vcc quad_perm:[2,3,0,1] row_mask:0xf bank_mask:0xf
	v_cndmask_b32_dpp v17, v15, v17, vcc quad_perm:[2,3,0,1] row_mask:0xf bank_mask:0xf
	v_cndmask_b32_dpp v64, v62, v64, vcc quad_perm:[2,3,0,1] row_mask:0xf bank_mask:0xf
	v_cndmask_b32_dpp v65, v63, v65, vcc quad_perm:[2,3,0,1] row_mask:0xf bank_mask:0xf
	s_mov_b32 vcc_lo, 0x33333333
	s_mov_b32 vcc_hi, 0x33333333
	s_nop 1
	v_cndmask_b32_dpp v14, v82, v14, vcc quad_perm:[2,3,0,1] row_mask:0xf bank_mask:0xf
	v_cndmask_b32_dpp v15, v83, v15, vcc quad_perm:[2,3,0,1] row_mask:0xf bank_mask:0xf
	v_cndmask_b32_dpp v62, v254, v62, vcc quad_perm:[2,3,0,1] row_mask:0xf bank_mask:0xf
	v_cndmask_b32_dpp v63, v255, v63, vcc quad_perm:[2,3,0,1] row_mask:0xf bank_mask:0xf
	v_cvt_pk_bf16_f32 v14, v14, v15
	v_cvt_pk_bf16_f32 v15, v16, v17
	v_cvt_pk_bf16_f32 v62, v62, v63
	v_cvt_pk_bf16_f32 v63, v64, v65
	global_store_dwordx2 v[252:253], v[14:15], off
	global_store_dwordx2 v[252:253], v[62:63], off offset:64
	v_mul_f32_e32 v46, v46, v78
	v_mul_f32_e32 v47, v47, v79
	v_mul_f32_e32 v48, v48, v80
	v_mul_f32_e32 v49, v49, v81
	v_mul_f32_e32 v30, v30, v78
	v_mul_f32_e32 v31, v31, v79
	v_mul_f32_e32 v32, v32, v80
	v_mul_f32_e32 v33, v33, v81
	s_mov_b32 vcc_lo, 0xaaaaaaaa
	s_mov_b32 vcc_hi, 0xaaaaaaaa
	s_nop 1
	v_mov_b32_e32 v82, v47
	v_mov_b32_e32 v83, v49
	v_mov_b32_e32 v254, v31
	v_mov_b32_e32 v255, v33
	v_cndmask_b32_dpp v47, v46, v47, vcc quad_perm:[1,0,3,2] row_mask:0xf bank_mask:0xf
	v_cndmask_b32_dpp v49, v48, v49, vcc quad_perm:[1,0,3,2] row_mask:0xf bank_mask:0xf
	v_cndmask_b32_dpp v31, v30, v31, vcc quad_perm:[1,0,3,2] row_mask:0xf bank_mask:0xf
	v_cndmask_b32_dpp v33, v32, v33, vcc quad_perm:[1,0,3,2] row_mask:0xf bank_mask:0xf
	s_mov_b32 vcc_lo, 0x55555555
	s_mov_b32 vcc_hi, 0x55555555
	s_nop 1
	v_cndmask_b32_dpp v46, v82, v46, vcc quad_perm:[1,0,3,2] row_mask:0xf bank_mask:0xf
	v_cndmask_b32_dpp v48, v83, v48, vcc quad_perm:[1,0,3,2] row_mask:0xf bank_mask:0xf
	v_cndmask_b32_dpp v30, v254, v30, vcc quad_perm:[1,0,3,2] row_mask:0xf bank_mask:0xf
	v_cndmask_b32_dpp v32, v255, v32, vcc quad_perm:[1,0,3,2] row_mask:0xf bank_mask:0xf
	s_mov_b32 vcc_lo, 0xcccccccc
	s_mov_b32 vcc_hi, 0xcccccccc
	s_nop 1
	v_mov_b32_e32 v82, v48
	v_mov_b32_e32 v83, v49
	v_mov_b32_e32 v254, v32
	v_mov_b32_e32 v255, v33
	v_cndmask_b32_dpp v48, v46, v48, vcc quad_perm:[2,3,0,1] row_mask:0xf bank_mask:0xf
	v_cndmask_b32_dpp v49, v47, v49, vcc quad_perm:[2,3,0,1] row_mask:0xf bank_mask:0xf
	v_cndmask_b32_dpp v32, v30, v32, vcc quad_perm:[2,3,0,1] row_mask:0xf bank_mask:0xf
	v_cndmask_b32_dpp v33, v31, v33, vcc quad_perm:[2,3,0,1] row_mask:0xf bank_mask:0xf
	s_mov_b32 vcc_lo, 0x33333333
	s_mov_b32 vcc_hi, 0x33333333
	s_nop 1
	v_cndmask_b32_dpp v46, v82, v46, vcc quad_perm:[2,3,0,1] row_mask:0xf bank_mask:0xf
	v_cndmask_b32_dpp v47, v83, v47, vcc quad_perm:[2,3,0,1] row_mask:0xf bank_mask:0xf
	v_cndmask_b32_dpp v30, v254, v30, vcc quad_perm:[2,3,0,1] row_mask:0xf bank_mask:0xf
	v_cndmask_b32_dpp v31, v255, v31, vcc quad_perm:[2,3,0,1] row_mask:0xf bank_mask:0xf
	v_cvt_pk_bf16_f32 v46, v46, v47
	v_cvt_pk_bf16_f32 v47, v48, v49
	v_cvt_pk_bf16_f32 v30, v30, v31
	v_cvt_pk_bf16_f32 v31, v32, v33
	global_store_dwordx2 v[252:253], v[46:47], off offset:128
	global_store_dwordx2 v[252:253], v[30:31], off offset:192
	s_add_i32 s75, s75, s33
	s_cmpk_gt_i32 s75, 0xff
	s_waitcnt vmcnt(63) expcnt(7) lgkmcnt(15)
	s_barrier
	s_cbranch_scc1 .LBB0_1707
